# v23 + P2a per-round cnt[e] loads hoisted to the loop preheader (scalar select per round) + P3 K/Q row-norm 8-lane sums via DPP instead of 3 ds_bpermute round trips
# speedup vs baseline: 1.0057x; 1.0057x over previous
.LBB0_258:
	v_readlane_b32 s7, v254, 0
	s_lshr_b32 s5, s7, 2
	s_and_b32 s4, s7, 7
	s_and_b32 s5, s5, 0x3ffffff8
	s_or_b32 s4, s5, s4
	s_sub_i32 s5, 63, s4
	s_lshl_b32 s4, s4, 2
	s_add_i32 s4, s4, 0
	s_add_i32 s6, s4, 0x21400
	v_mov_b32_e32 v2, s6
	s_waitcnt lgkmcnt(0)
	s_barrier
	ds_read_b32 v2, v2
	s_lshl_b32 s5, s5, 2
	s_add_i32 s5, s5, 0
	s_add_i32 s4, s4, 0x21600
	s_add_i32 s6, s5, 0x21500
	v_mov_b32_e32 v4, s4
	s_add_i32 s4, s5, 0x21700
	v_mov_b32_e32 v3, s6
	v_mov_b32_e32 v5, s4
	ds_read_b32 v3, v3
	ds_read_b32 v4, v4
	ds_read_b32 v5, v5
	s_waitcnt lgkmcnt(3)
	v_readfirstlane_b32 s33, v2
	s_lshl_b32 s4, s33, 2
	s_add_i32 s5, 0, 0x21000
	s_add_i32 s4, s5, s4
	s_waitcnt lgkmcnt(2)
	v_readfirstlane_b32 s36, v3
	v_mov_b32_e32 v2, s4
	s_lshl_b32 s4, s36, 2
	s_add_i32 s4, s5, s4
	s_waitcnt lgkmcnt(1)
	v_readfirstlane_b32 s37, v4
	v_mov_b32_e32 v3, s4
	s_lshl_b32 s4, s37, 2
	s_add_i32 s4, s5, s4
	s_waitcnt lgkmcnt(0)
	v_readfirstlane_b32 s54, v5
	v_mov_b32_e32 v4, s4
	s_lshl_b32 s4, s54, 2
	s_add_i32 s4, s5, s4
	v_mov_b32_e32 v5, s4
	s_bfe_u32 s8, s7, 0x20003
	ds_read_b32 v2, v2
	ds_read_b32 v3, v3
	ds_read_b32 v4, v4
	ds_read_b32 v5, v5
	s_waitcnt lgkmcnt(0)
	s_barrier
	s_bitcmp0_b32 s7, 5
	s_load_dwordx4 s[12:15], s[0:1], 0x120
	s_load_dwordx2 s[6:7], s[0:1], 0x140
	s_load_dwordx2 s[16:17], s[0:1], 0x58
	s_load_dwordx2 s[18:19], s[0:1], 0xd8
	s_cselect_b64 s[4:5], -1, 0
	s_lshl_b32 s9, s8, 8
	s_add_i32 s10, s9, 0x300
	s_lshl_b32 s8, s8, 7
	s_waitcnt lgkmcnt(0)
	s_add_u32 s20, s6, s8
	s_mov_b32 s55, 0
	v_readfirstlane_b32 s56, v2
	v_readfirstlane_b32 s57, v3
	v_readfirstlane_b32 s58, v4
	v_readfirstlane_b32 s59, v5
	s_addc_u32 s21, s7, 0
	v_mov_b32_e32 v163, 0
	v_lshlrev_b32_e64 v244, 2, s33
	v_lshlrev_b32_e64 v245, 2, s36
	v_lshlrev_b32_e64 v246, 2, s37
	v_lshlrev_b32_e64 v247, 2, s54
	global_load_dword v244, v244, s[2:3]
	global_load_dword v245, v245, s[2:3]
	global_load_dword v246, v246, s[2:3]
	global_load_dword v247, v247, s[2:3]
	s_waitcnt vmcnt(0)
	v_readfirstlane_b32 s98, v244
	v_readfirstlane_b32 s99, v245
	v_readfirstlane_b32 s100, v246
	v_readfirstlane_b32 s101, v247
	s_movk_i32 s60, 0xf800
	v_mov_b32_e32 v166, s10
	v_mov_b32_e32 v167, s9
	s_add_i32 s61, 0, 0x20000
	s_branch .LBB0_260

.LBB0_260:
	s_sub_i32 s8, 3, s55
	s_and_b64 s[6:7], s[4:5], exec
	s_cselect_b32 s22, s55, s8
	s_cmp_eq_u32 s22, 2
	s_cselect_b64 s[8:9], -1, 0
	s_and_b64 s[6:7], s[8:9], exec
	s_cselect_b32 s23, s37, s54
	s_cmp_eq_u32 s22, 1
	s_cselect_b64 s[10:11], -1, 0
	s_and_b64 s[6:7], s[10:11], exec
	s_cselect_b32 s24, s36, s23
	s_cmp_eq_u32 s22, 0
	s_cselect_b64 s[22:23], -1, 0
	s_and_b64 s[6:7], s[22:23], exec
	s_cselect_b32 s6, s33, s24
	s_ashr_i32 s7, s6, 31
	s_and_b64 s[24:25], s[8:9], exec
	s_cselect_b32 s62, s100, s101
	s_and_b64 s[24:25], s[10:11], exec
	s_cselect_b32 s62, s99, s62
	s_and_b64 s[24:25], s[22:23], exec
	s_cselect_b32 s62, s98, s62
	s_cmp_lt_i32 s62, 1
	s_cbranch_scc1 .LBB0_259
	s_and_b64 s[8:9], s[8:9], exec
	s_cselect_b32 s24, s58, s59
	s_and_b64 s[8:9], s[10:11], exec
	s_cselect_b32 s10, s57, s24
	s_and_b64 s[8:9], s[22:23], exec
	s_cselect_b32 s63, s56, s10
	s_lshl_b64 s[8:9], s[6:7], 21
	s_add_u32 s22, s16, s8
	s_addc_u32 s23, s17, s9
	s_lshl_b64 s[6:7], s[6:7], 16
	s_add_u32 s24, s12, s6
	s_addc_u32 s25, s13, s7
	s_add_u32 s26, s14, s6
	s_addc_u32 s27, s15, s7
	s_add_u32 s28, s22, 0x1000
	s_addc_u32 s29, s23, 0
	s_add_u32 s30, s22, 0x20000
	s_addc_u32 s31, s23, 0
	s_add_u32 s34, s22, 0x21000
	s_addc_u32 s35, s23, 0
	s_add_u32 s38, s22, 0x40000
	s_addc_u32 s39, s23, 0
	s_add_u32 s40, s22, 0x41000
	s_addc_u32 s41, s23, 0
	s_mov_b32 s64, 0
	s_branch .LBB0_263

.LBB0_509:
	s_add_i32 s37, s3, -8
	s_add_i32 s23, s5, 4
	s_and_b32 s39, s37, 0x7c
	s_cmp_lt_u32 s5, 28
	s_cselect_b64 s[88:89], -1, 0
	s_min_u32 s37, s23, 31
	s_add_i32 s37, s37, s96
	s_and_b32 s37, s37, 31
	s_waitcnt vmcnt(15) lgkmcnt(3)
	v_mfma_f32_16x16x32_bf16 v[190:193], v[114:117], v[194:197], v[190:193]
	s_lshl_b32 s45, s37, 6
	s_waitcnt lgkmcnt(2)
	v_mfma_f32_16x16x32_bf16 v[110:113], v[114:117], v[198:201], v[110:113]
	s_waitcnt lgkmcnt(1)
	v_mfma_f32_16x16x32_bf16 v[94:97], v[114:117], v[206:209], v[94:97]
	s_waitcnt lgkmcnt(0)
	v_mfma_f32_16x16x32_bf16 v[62:65], v[114:117], v[202:205], v[62:65]
	v_cndmask_b32_e64 v114, v216, 0, s[88:89]
	v_sub_u32_e32 v114, s45, v114
	v_ashrrev_i32_e32 v115, 31, v114
	v_lshl_add_u64 v[114:115], v[114:115], 4, v[218:219]
	s_waitcnt vmcnt(14)
	v_mfma_f32_16x16x32_bf16 v[186:189], v[118:121], v[194:197], v[186:189]
	v_mfma_f32_16x16x32_bf16 v[106:109], v[118:121], v[198:201], v[106:109]
	v_mfma_f32_16x16x32_bf16 v[90:93], v[118:121], v[206:209], v[90:93]
	v_mfma_f32_16x16x32_bf16 v[58:61], v[118:121], v[202:205], v[58:61]
	v_add_co_u32_e32 v118, vcc, s40, v114
	s_nop 1
	v_addc_co_u32_e32 v119, vcc, 0, v115, vcc
	s_waitcnt vmcnt(12)
	v_mfma_f32_16x16x32_bf16 v[170:173], v[122:125], v[194:197], v[170:173]
	v_mfma_f32_16x16x32_bf16 v[98:101], v[122:125], v[198:201], v[98:101]
	v_mfma_f32_16x16x32_bf16 v[82:85], v[122:125], v[206:209], v[82:85]
	v_mfma_f32_16x16x32_bf16 v[50:53], v[122:125], v[202:205], v[50:53]
	v_add_co_u32_e32 v122, vcc, s41, v114
	s_nop 1
	v_addc_co_u32_e32 v123, vcc, 0, v115, vcc
	v_add_co_u32_e32 v124, vcc, s8, v114
	v_mfma_f32_16x16x32_bf16 v[182:185], v[126:129], v[194:197], v[182:185]
	s_nop 0
	v_addc_co_u32_e32 v125, vcc, 0, v115, vcc
	v_bitop3_b32 v194, s39, v242, v243 bitop3:0x36
	v_mfma_f32_16x16x32_bf16 v[102:105], v[126:129], v[198:201], v[102:105]
	v_mfma_f32_16x16x32_bf16 v[86:89], v[126:129], v[206:209], v[86:89]
	v_mfma_f32_16x16x32_bf16 v[54:57], v[126:129], v[202:205], v[54:57]
	global_load_dwordx4 v[114:117], v[114:115], off
	s_nop 0
	global_load_dwordx4 v[118:121], v[118:119], off
	s_nop 0
	global_load_dwordx4 v[126:129], v[122:123], off
	s_nop 0
	global_load_dwordx4 v[122:125], v[124:125], off
	v_lshl_add_u32 v202, v194, 4, v244
	v_add_u32_e32 v203, 0x10000, v202
	v_add_u32_e32 v206, 0x18000, v202
	ds_read_b128 v[194:197], v202
	ds_read_b128 v[198:201], v202 offset:32768
	ds_read_b128 v[202:205], v203
	ds_read_b128 v[206:209], v206
	s_min_u32 s45, s5, 26
	s_add_i32 s45, s45, s93
	s_add_i32 s39, s3, -4
	s_lshl_b32 s45, s45, 6
	s_and_b32 s39, s39, 0x7c
	s_and_b32 s45, s45, 0x7c0
	s_cmp_gt_u32 s5, 26
	s_cselect_b64 vcc, -1, 0
	s_waitcnt vmcnt(15) lgkmcnt(3)
	v_mfma_f32_16x16x32_bf16 v[190:193], v[130:133], v[194:197], v[190:193]
	s_waitcnt lgkmcnt(2)
	v_mfma_f32_16x16x32_bf16 v[110:113], v[130:133], v[198:201], v[110:113]
	s_waitcnt lgkmcnt(1)
	v_mfma_f32_16x16x32_bf16 v[94:97], v[130:133], v[202:205], v[94:97]
	s_waitcnt lgkmcnt(0)
	v_mfma_f32_16x16x32_bf16 v[62:65], v[130:133], v[206:209], v[62:65]
	v_cndmask_b32_e32 v130, 0, v216, vcc
	v_sub_u32_e32 v130, s45, v130
	v_ashrrev_i32_e32 v131, 31, v130
	v_lshl_add_u64 v[130:131], v[130:131], 4, v[218:219]
	s_waitcnt vmcnt(14)
	v_mfma_f32_16x16x32_bf16 v[186:189], v[134:137], v[194:197], v[186:189]
	v_mfma_f32_16x16x32_bf16 v[106:109], v[134:137], v[198:201], v[106:109]
	v_mfma_f32_16x16x32_bf16 v[90:93], v[134:137], v[202:205], v[90:93]
	v_mfma_f32_16x16x32_bf16 v[58:61], v[134:137], v[206:209], v[58:61]
	v_add_co_u32_e32 v134, vcc, s40, v130
	s_nop 1
	v_addc_co_u32_e32 v135, vcc, 0, v131, vcc
	s_waitcnt vmcnt(12)
	v_mfma_f32_16x16x32_bf16 v[170:173], v[138:141], v[194:197], v[170:173]
	v_mfma_f32_16x16x32_bf16 v[98:101], v[138:141], v[198:201], v[98:101]
	v_mfma_f32_16x16x32_bf16 v[82:85], v[138:141], v[202:205], v[82:85]
	v_mfma_f32_16x16x32_bf16 v[50:53], v[138:141], v[206:209], v[50:53]
	v_add_co_u32_e32 v138, vcc, s41, v130
	s_nop 1
	v_addc_co_u32_e32 v139, vcc, 0, v131, vcc
	v_add_co_u32_e32 v140, vcc, s8, v130
	v_mfma_f32_16x16x32_bf16 v[182:185], v[142:145], v[194:197], v[182:185]
	s_nop 0
	v_addc_co_u32_e32 v141, vcc, 0, v131, vcc
	v_bitop3_b32 v194, s39, v242, v243 bitop3:0x36
	v_mfma_f32_16x16x32_bf16 v[102:105], v[142:145], v[198:201], v[102:105]
	v_mfma_f32_16x16x32_bf16 v[86:89], v[142:145], v[202:205], v[86:89]
	v_lshl_add_u32 v202, v194, 4, v244
	v_add_u32_e32 v203, 0x10000, v202
	v_mfma_f32_16x16x32_bf16 v[54:57], v[142:145], v[206:209], v[54:57]
	global_load_dwordx4 v[130:133], v[130:131], off
	s_nop 0
	global_load_dwordx4 v[134:137], v[134:135], off
	s_nop 0
	global_load_dwordx4 v[142:145], v[138:139], off
	s_nop 0
	global_load_dwordx4 v[138:141], v[140:141], off
	v_add_u32_e32 v206, 0x18000, v202
	ds_read_b128 v[194:197], v202
	ds_read_b128 v[198:201], v202 offset:32768
	ds_read_b128 v[202:205], v203
	ds_read_b128 v[206:209], v206
	s_min_u32 s45, s5, 25
	s_add_i32 s45, s45, s34
	s_lshl_b32 s45, s45, 6
	s_and_b32 s39, s3, 0x7c
	s_and_b32 s45, s45, 0x7c0
	s_cmp_gt_u32 s5, 25
	s_cselect_b64 vcc, -1, 0
	s_waitcnt vmcnt(15) lgkmcnt(3)
	v_mfma_f32_16x16x32_bf16 v[190:193], v[146:149], v[194:197], v[190:193]
	s_waitcnt lgkmcnt(2)
	v_mfma_f32_16x16x32_bf16 v[110:113], v[146:149], v[198:201], v[110:113]
	s_waitcnt lgkmcnt(1)
	v_mfma_f32_16x16x32_bf16 v[94:97], v[146:149], v[202:205], v[94:97]
	s_waitcnt lgkmcnt(0)
	v_mfma_f32_16x16x32_bf16 v[62:65], v[146:149], v[206:209], v[62:65]
	v_cndmask_b32_e32 v146, 0, v216, vcc
	v_sub_u32_e32 v146, s45, v146
	v_ashrrev_i32_e32 v147, 31, v146
	v_lshl_add_u64 v[146:147], v[146:147], 4, v[218:219]
	s_waitcnt vmcnt(14)
	v_mfma_f32_16x16x32_bf16 v[186:189], v[150:153], v[194:197], v[186:189]
	v_mfma_f32_16x16x32_bf16 v[106:109], v[150:153], v[198:201], v[106:109]
	v_mfma_f32_16x16x32_bf16 v[90:93], v[150:153], v[202:205], v[90:93]
	v_mfma_f32_16x16x32_bf16 v[58:61], v[150:153], v[206:209], v[58:61]
	v_add_co_u32_e32 v150, vcc, s40, v146
	s_nop 1
	v_addc_co_u32_e32 v151, vcc, 0, v147, vcc
	s_waitcnt vmcnt(12)
	v_mfma_f32_16x16x32_bf16 v[170:173], v[154:157], v[194:197], v[170:173]
	v_mfma_f32_16x16x32_bf16 v[98:101], v[154:157], v[198:201], v[98:101]
	v_mfma_f32_16x16x32_bf16 v[82:85], v[154:157], v[202:205], v[82:85]
	v_mfma_f32_16x16x32_bf16 v[50:53], v[154:157], v[206:209], v[50:53]
	v_add_co_u32_e32 v154, vcc, s41, v146
	s_nop 1
	v_addc_co_u32_e32 v155, vcc, 0, v147, vcc
	v_add_co_u32_e32 v156, vcc, s8, v146
	v_mfma_f32_16x16x32_bf16 v[182:185], v[158:161], v[194:197], v[182:185]
	s_nop 0
	v_addc_co_u32_e32 v157, vcc, 0, v147, vcc
	v_bitop3_b32 v194, s39, v242, v243 bitop3:0x36
	v_mfma_f32_16x16x32_bf16 v[102:105], v[158:161], v[198:201], v[102:105]
	v_mfma_f32_16x16x32_bf16 v[86:89], v[158:161], v[202:205], v[86:89]
	v_lshl_add_u32 v202, v194, 4, v244
	v_add_u32_e32 v203, 0x10000, v202
	v_mfma_f32_16x16x32_bf16 v[54:57], v[158:161], v[206:209], v[54:57]
	global_load_dwordx4 v[146:149], v[146:147], off
	s_nop 0
	global_load_dwordx4 v[150:153], v[150:151], off
	s_nop 0
	global_load_dwordx4 v[158:161], v[154:155], off
	s_nop 0
	global_load_dwordx4 v[154:157], v[156:157], off
	v_add_u32_e32 v206, 0x18000, v202
	ds_read_b128 v[194:197], v202
	ds_read_b128 v[198:201], v202 offset:32768
	ds_read_b128 v[202:205], v203
	ds_read_b128 v[206:209], v206
	s_min_u32 s39, s5, 24
	s_add_i32 s39, s39, s35
	s_lshl_b32 s39, s39, 6
	s_lshl_b32 s37, s37, 2
	s_and_b32 s39, s39, 0x7c0
	s_cmp_gt_u32 s5, 24
	s_cselect_b64 vcc, -1, 0
	s_waitcnt vmcnt(15) lgkmcnt(3)
	v_mfma_f32_16x16x32_bf16 v[190:193], v[162:165], v[194:197], v[190:193]
	s_waitcnt lgkmcnt(2)
	v_mfma_f32_16x16x32_bf16 v[110:113], v[162:165], v[198:201], v[110:113]
	s_waitcnt lgkmcnt(1)
	v_mfma_f32_16x16x32_bf16 v[94:97], v[162:165], v[202:205], v[94:97]
	s_waitcnt lgkmcnt(0)
	v_mfma_f32_16x16x32_bf16 v[62:65], v[162:165], v[206:209], v[62:65]
	v_cndmask_b32_e32 v162, 0, v216, vcc
	v_sub_u32_e32 v162, s39, v162
	v_ashrrev_i32_e32 v163, 31, v162
	v_lshl_add_u64 v[162:163], v[162:163], 4, v[218:219]
	s_waitcnt vmcnt(14)
	v_mfma_f32_16x16x32_bf16 v[186:189], v[166:169], v[194:197], v[186:189]
	v_mfma_f32_16x16x32_bf16 v[106:109], v[166:169], v[198:201], v[106:109]
	v_mfma_f32_16x16x32_bf16 v[90:93], v[166:169], v[202:205], v[90:93]
	v_mfma_f32_16x16x32_bf16 v[58:61], v[166:169], v[206:209], v[58:61]
	v_add_co_u32_e32 v166, vcc, s40, v162
	s_nop 1
	v_addc_co_u32_e32 v167, vcc, 0, v163, vcc
	s_waitcnt vmcnt(12)
	v_mfma_f32_16x16x32_bf16 v[170:173], v[174:177], v[194:197], v[170:173]
	v_mfma_f32_16x16x32_bf16 v[98:101], v[174:177], v[198:201], v[98:101]
	v_mfma_f32_16x16x32_bf16 v[82:85], v[174:177], v[202:205], v[82:85]
	v_mfma_f32_16x16x32_bf16 v[50:53], v[174:177], v[206:209], v[50:53]
	v_add_co_u32_e32 v174, vcc, s41, v162
	s_nop 1
	v_addc_co_u32_e32 v175, vcc, 0, v163, vcc
	v_add_co_u32_e32 v176, vcc, s8, v162
	v_mfma_f32_16x16x32_bf16 v[182:185], v[178:181], v[194:197], v[182:185]
	s_nop 0
	v_addc_co_u32_e32 v177, vcc, 0, v163, vcc
	v_bitop3_b32 v194, s37, v242, v243 bitop3:0x36
	v_mfma_f32_16x16x32_bf16 v[102:105], v[178:181], v[198:201], v[102:105]
	v_mfma_f32_16x16x32_bf16 v[86:89], v[178:181], v[202:205], v[86:89]
	v_lshl_add_u32 v202, v194, 4, v244
	v_add_u32_e32 v203, 0x10000, v202
	v_mfma_f32_16x16x32_bf16 v[54:57], v[178:181], v[206:209], v[54:57]
	global_load_dwordx4 v[162:165], v[162:163], off
	s_nop 0
	global_load_dwordx4 v[166:169], v[166:167], off
	s_nop 0
	global_load_dwordx4 v[178:181], v[174:175], off
	s_nop 0
	global_load_dwordx4 v[174:177], v[176:177], off
	ds_read_b128 v[194:197], v202
	ds_read_b128 v[198:201], v202 offset:32768
	v_add_u32_e32 v202, 0x18000, v202
	ds_read_b128 v[206:209], v203
	ds_read_b128 v[202:205], v202
	s_add_i32 s3, s3, 16
	s_and_b64 vcc, exec, s[88:89]
	s_mov_b32 s5, s23
	s_cbranch_vccnz .LBB0_509
	s_and_b64 s[86:87], s[86:87], exec
	s_movk_i32 s3, 0xf8
	s_cselect_b32 s3, s3, 0x100
	s_cmp_eq_u32 s75, 0
	s_cselect_b64 s[86:87], -1, 0
	s_and_b64 s[88:89], s[86:87], exec
	s_cselect_b32 s3, 0xf0, s3
	v_readlane_b32 s88, v254, 19
	v_readlane_b32 s89, v254, 20
	s_add_u32 s88, s88, s3
	s_addc_u32 s89, s89, 0
	s_waitcnt vmcnt(15)
	v_mov_b32_e32 v115, v229
	s_load_dwordx2 s[88:89], s[88:89], 0x0
	v_cndmask_b32_e64 v114, 1.0, v225, s[12:13]
	s_waitcnt vmcnt(14)
	v_lshlrev_b32_e32 v120, 7, v115
	v_lshrrev_b32_e32 v121, 1, v115
	v_bfe_u32 v116, v115, 3, 3
	v_and_b32_e32 v120, 0x780, v120
	v_and_b32_e32 v121, 8, v121
	v_or_b32_e32 v118, s0, v116
	s_waitcnt vmcnt(12)
	v_add3_u32 v123, s73, v120, v121
	v_lshl_add_u32 v120, v116, 7, s73
	v_bitop3_b32 v116, v116, v115, 7 bitop3:0x78
	v_lshlrev_b32_e32 v116, 4, v116
	v_pk_mul_f32 v[78:79], v[114:115], v[78:79] op_sel_hi:[0,1]
	v_pk_mul_f32 v[74:75], v[114:115], v[74:75] op_sel_hi:[0,1]
	v_and_b32_e32 v117, 7, v115
	v_bfe_u32 v122, v115, 5, 1
	v_add_u32_e32 v116, v120, v116
	v_cvt_pk_bf16_f32 v120, v78, v79
	v_pk_mul_f32 v[78:79], v[114:115], v[80:81] op_sel_hi:[0,1]
	v_cvt_pk_bf16_f32 v80, v74, v75
	v_pk_mul_f32 v[74:75], v[114:115], v[76:77] op_sel_hi:[0,1]
	v_pk_mul_f32 v[70:71], v[114:115], v[70:71] op_sel_hi:[0,1]
	v_pk_mul_f32 v[72:73], v[114:115], v[72:73] op_sel_hi:[0,1]
	v_pk_mul_f32 v[66:67], v[114:115], v[66:67] op_sel_hi:[0,1]
	v_pk_mul_f32 v[68:69], v[114:115], v[68:69] op_sel_hi:[0,1]
	v_cvt_pk_bf16_f32 v121, v78, v79
	v_bitop3_b32 v78, v122, v115, 7 bitop3:0x78
	v_cvt_pk_bf16_f32 v81, v74, v75
	v_bitop3_b32 v74, v122, v117, 2 bitop3:0x36
	v_cvt_pk_bf16_f32 v70, v70, v71
	v_cvt_pk_bf16_f32 v71, v72, v73
	v_bitop3_b32 v72, v122, v117, 4 bitop3:0x36
	v_cvt_pk_bf16_f32 v66, v66, v67
	v_cvt_pk_bf16_f32 v67, v68, v69
	v_bitop3_b32 v68, v122, v117, 6 bitop3:0x36
	v_lshlrev_b32_e32 v78, 4, v78
	v_lshlrev_b32_e32 v74, 4, v74
	v_lshlrev_b32_e32 v72, 4, v72
	v_lshlrev_b32_e32 v68, 4, v68
	v_add_u32_e32 v78, v123, v78
	v_add_u32_e32 v74, v123, v74
	v_add_u32_e32 v73, v123, v72
	v_add_u32_e32 v75, v123, v68
	ds_write_b64 v78, v[120:121]
	ds_write_b64 v74, v[80:81]
	ds_write_b64 v73, v[70:71]
	ds_write_b64 v75, v[66:67]
	s_waitcnt lgkmcnt(0)
	ds_read_b128 v[66:69], v116
	s_waitcnt lgkmcnt(0)
	s_add_u32 s88, s88, s16
	v_ashrrev_i32_e32 v119, 31, v118
	s_addc_u32 s89, s89, s17
	v_lshlrev_b64 v[70:71], 11, v[118:119]
	v_lshl_add_u64 v[70:71], s[88:89], 0, v[70:71]
	v_lshlrev_b32_e32 v210, 4, v117
	v_cndmask_b32_e64 v72, 0, 1, s[18:19]
	v_lshl_add_u64 v[70:71], v[70:71], 0, v[210:211]
	v_cmp_ne_u32_e64 s[12:13], 1, v72
	s_andn2_b64 vcc, exec, s[18:19]
	v_mov_b32_e32 v72, 0
	global_store_dwordx4 v[70:71], v[66:69], off
	s_cbranch_vccnz .LBB0_512
	v_lshlrev_b32_e32 v72, 16, v66
	v_and_b32_e32 v66, 0xffff0000, v66
	v_fma_f32 v72, v72, v72, 0
	v_fmac_f32_e32 v72, v66, v66
	v_lshlrev_b32_e32 v66, 16, v67
	v_and_b32_e32 v67, 0xffff0000, v67
	v_fmac_f32_e32 v72, v66, v66
	v_fmac_f32_e32 v72, v67, v67
	v_lshlrev_b32_e32 v66, 16, v68
	v_and_b32_e32 v67, 0xffff0000, v68
	v_fmac_f32_e32 v72, v66, v66
	v_fmac_f32_e32 v72, v67, v67
	v_lshlrev_b32_e32 v66, 16, v69
	v_and_b32_e32 v67, 0xffff0000, v69
	v_fmac_f32_e32 v72, v66, v66
	v_fmac_f32_e32 v72, v67, v67
	s_nop 1
	v_add_f32_dpp v66, v72, v72 quad_perm:[1,0,3,2] row_mask:0xf bank_mask:0xf
	s_waitcnt lgkmcnt(0)
	s_nop 1
	v_add_f32_dpp v66, v66, v66 quad_perm:[2,3,0,1] row_mask:0xf bank_mask:0xf
	s_nop 1
	v_add_f32_dpp v66, v66, v66 row_half_mirror row_mask:0xf bank_mask:0xf
	v_max_f32_e32 v72, 0, v66
.LBB0_512:
	ds_read_b128 v[66:69], v116 offset:1024
	v_add_co_u32_e32 v76, vcc, 0x4000, v70
	s_nop 1
	v_addc_co_u32_e32 v77, vcc, 0, v71, vcc
	s_and_b64 vcc, exec, s[12:13]
	s_waitcnt lgkmcnt(0)
	global_store_dwordx4 v[76:77], v[66:69], off
	s_cbranch_vccnz .LBB0_514
	v_lshlrev_b32_e32 v76, 16, v66
	v_and_b32_e32 v66, 0xffff0000, v66
	v_fma_f32 v76, v76, v76, 0
	v_fmac_f32_e32 v76, v66, v66
	v_lshlrev_b32_e32 v66, 16, v67
	v_and_b32_e32 v67, 0xffff0000, v67
	v_fmac_f32_e32 v76, v66, v66
	v_fmac_f32_e32 v76, v67, v67
	v_lshlrev_b32_e32 v66, 16, v68
	v_and_b32_e32 v67, 0xffff0000, v68
	v_fmac_f32_e32 v76, v66, v66
	v_fmac_f32_e32 v76, v67, v67
	v_lshlrev_b32_e32 v66, 16, v69
	v_and_b32_e32 v67, 0xffff0000, v69
	v_fmac_f32_e32 v76, v66, v66
	v_fmac_f32_e32 v76, v67, v67
	s_nop 1
	v_add_f32_dpp v66, v76, v76 quad_perm:[1,0,3,2] row_mask:0xf bank_mask:0xf
	s_waitcnt lgkmcnt(0)
	s_nop 1
	v_add_f32_dpp v66, v66, v66 quad_perm:[2,3,0,1] row_mask:0xf bank_mask:0xf
	s_nop 1
	v_add_f32_dpp v66, v66, v66 row_half_mirror row_mask:0xf bank_mask:0xf
	v_max_f32_e32 v67, v72, v72
	v_max_f32_e32 v72, v67, v66
.LBB0_514:
	v_mov_b32_e32 v115, v114
	v_pk_mul_f32 v[66:67], v[114:115], v[190:191]
	v_pk_mul_f32 v[68:69], v[114:115], v[192:193]
	v_cvt_pk_bf16_f32 v66, v66, v67
	v_cvt_pk_bf16_f32 v67, v68, v69
	s_waitcnt lgkmcnt(0)
	ds_write_b64 v78, v[66:67]
	v_pk_mul_f32 v[66:67], v[114:115], v[186:187]
	v_pk_mul_f32 v[68:69], v[114:115], v[188:189]
	v_cvt_pk_bf16_f32 v66, v66, v67
	v_cvt_pk_bf16_f32 v67, v68, v69
	ds_write_b64 v74, v[66:67]
	v_pk_mul_f32 v[66:67], v[114:115], v[182:183]
	v_pk_mul_f32 v[68:69], v[114:115], v[184:185]
	v_cvt_pk_bf16_f32 v66, v66, v67
	v_cvt_pk_bf16_f32 v67, v68, v69
	ds_write_b64 v73, v[66:67]
	v_pk_mul_f32 v[66:67], v[114:115], v[170:171]
	v_pk_mul_f32 v[68:69], v[114:115], v[172:173]
	v_cvt_pk_bf16_f32 v66, v66, v67
	v_cvt_pk_bf16_f32 v67, v68, v69
	ds_write_b64 v75, v[66:67]
	s_waitcnt lgkmcnt(0)
	ds_read_b128 v[66:69], v116
	s_and_b64 vcc, exec, s[12:13]
	v_mov_b32_e32 v73, 0
	s_waitcnt lgkmcnt(0)
	global_store_dwordx4 v[70:71], v[66:69], off offset:128
	s_cbranch_vccnz .LBB0_516
	v_lshlrev_b32_e32 v73, 16, v66
	v_and_b32_e32 v66, 0xffff0000, v66
	v_fma_f32 v73, v73, v73, 0
	v_fmac_f32_e32 v73, v66, v66
	v_lshlrev_b32_e32 v66, 16, v67
	v_and_b32_e32 v67, 0xffff0000, v67
	v_fmac_f32_e32 v73, v66, v66
	v_fmac_f32_e32 v73, v67, v67
	v_lshlrev_b32_e32 v66, 16, v68
	v_and_b32_e32 v67, 0xffff0000, v68
	v_fmac_f32_e32 v73, v66, v66
	v_fmac_f32_e32 v73, v67, v67
	v_lshlrev_b32_e32 v66, 16, v69
	v_and_b32_e32 v67, 0xffff0000, v69
	v_fmac_f32_e32 v73, v66, v66
	v_fmac_f32_e32 v73, v67, v67
	s_nop 1
	v_add_f32_dpp v66, v73, v73 quad_perm:[1,0,3,2] row_mask:0xf bank_mask:0xf
	s_waitcnt lgkmcnt(0)
	s_nop 1
	v_add_f32_dpp v66, v66, v66 quad_perm:[2,3,0,1] row_mask:0xf bank_mask:0xf
	s_nop 1
	v_add_f32_dpp v66, v66, v66 row_half_mirror row_mask:0xf bank_mask:0xf
	v_max_f32_e32 v73, 0, v66
.LBB0_516:
	ds_read_b128 v[66:69], v116 offset:1024
	v_add_co_u32_e32 v70, vcc, 0x4000, v70
	s_nop 1
	v_addc_co_u32_e32 v71, vcc, 0, v71, vcc
	s_and_b64 vcc, exec, s[12:13]
	s_waitcnt lgkmcnt(0)
	global_store_dwordx4 v[70:71], v[66:69], off offset:128
	s_cbranch_vccnz .LBB0_518
	v_lshlrev_b32_e32 v70, 16, v66
	v_and_b32_e32 v66, 0xffff0000, v66
	v_fma_f32 v70, v70, v70, 0
	v_fmac_f32_e32 v70, v66, v66
	v_lshlrev_b32_e32 v66, 16, v67
	v_and_b32_e32 v67, 0xffff0000, v67
	v_fmac_f32_e32 v70, v66, v66
	v_fmac_f32_e32 v70, v67, v67
	v_lshlrev_b32_e32 v66, 16, v68
	v_and_b32_e32 v67, 0xffff0000, v68
	v_fmac_f32_e32 v70, v66, v66
	v_fmac_f32_e32 v70, v67, v67
	v_lshlrev_b32_e32 v66, 16, v69
	v_and_b32_e32 v67, 0xffff0000, v69
	v_fmac_f32_e32 v70, v66, v66
	v_fmac_f32_e32 v70, v67, v67
	s_nop 1
	v_add_f32_dpp v66, v70, v70 quad_perm:[1,0,3,2] row_mask:0xf bank_mask:0xf
	s_waitcnt lgkmcnt(0)
	s_nop 1
	v_add_f32_dpp v66, v66, v66 quad_perm:[2,3,0,1] row_mask:0xf bank_mask:0xf
	s_nop 1
	v_add_f32_dpp v66, v66, v66 row_half_mirror row_mask:0xf bank_mask:0xf
	v_max_f32_e32 v67, v73, v73
	v_max_f32_e32 v73, v67, v66
.LBB0_518:
	v_mov_b32_e32 v74, v229
	s_waitcnt lgkmcnt(0)
	v_pk_mul_f32 v[46:47], v[114:115], v[46:47]
	v_bfe_u32 v70, v74, 3, 3
	v_or_b32_e32 v66, s64, v70
	v_ashrrev_i32_e32 v67, 31, v66
	v_lshlrev_b64 v[68:69], 11, v[66:67]
	v_lshlrev_b32_e32 v66, 7, v74
	v_lshrrev_b32_e32 v71, 1, v74
	v_and_b32_e32 v66, 0x780, v66
	v_and_b32_e32 v71, 8, v71
	v_add3_u32 v76, s73, v66, v71
	v_lshl_add_u32 v66, v70, 7, s73
	v_bitop3_b32 v70, v70, v74, 7 bitop3:0x78
	v_lshlrev_b32_e32 v70, 4, v70
	v_pk_mul_f32 v[42:43], v[114:115], v[42:43]
	v_and_b32_e32 v67, 7, v74
	v_bfe_u32 v75, v74, 5, 1
	v_add_u32_e32 v66, v66, v70
	v_cvt_pk_bf16_f32 v70, v46, v47
	v_pk_mul_f32 v[46:47], v[114:115], v[48:49]
	v_cvt_pk_bf16_f32 v48, v42, v43
	v_pk_mul_f32 v[42:43], v[114:115], v[44:45]
	v_pk_mul_f32 v[38:39], v[114:115], v[38:39]
	v_pk_mul_f32 v[40:41], v[114:115], v[40:41]
	v_pk_mul_f32 v[34:35], v[114:115], v[34:35]
	v_pk_mul_f32 v[36:37], v[114:115], v[36:37]
	v_cvt_pk_bf16_f32 v71, v46, v47
	v_bitop3_b32 v46, v75, v74, 7 bitop3:0x78
	v_cvt_pk_bf16_f32 v49, v42, v43
	v_bitop3_b32 v42, v75, v67, 2 bitop3:0x36
	v_cvt_pk_bf16_f32 v38, v38, v39
	v_cvt_pk_bf16_f32 v39, v40, v41
	v_bitop3_b32 v40, v75, v67, 4 bitop3:0x36
	v_cvt_pk_bf16_f32 v34, v34, v35
	v_cvt_pk_bf16_f32 v35, v36, v37
	v_bitop3_b32 v36, v75, v67, 6 bitop3:0x36
	v_lshlrev_b32_e32 v46, 4, v46
	v_lshlrev_b32_e32 v42, 4, v42
	v_lshlrev_b32_e32 v40, 4, v40
	v_lshlrev_b32_e32 v36, 4, v36
	v_add_u32_e32 v46, v76, v46
	v_add_u32_e32 v42, v76, v42
	v_add_u32_e32 v40, v76, v40
	v_add_u32_e32 v41, v76, v36
	ds_write_b64 v46, v[70:71]
	ds_write_b64 v42, v[48:49]
	ds_write_b64 v40, v[38:39]
	ds_write_b64 v41, v[34:35]
	s_waitcnt lgkmcnt(0)
	ds_read_b128 v[34:37], v66
	v_lshl_add_u64 v[38:39], s[88:89], 0, v[68:69]
	v_lshlrev_b32_e32 v210, 4, v67
	v_lshl_add_u64 v[38:39], v[38:39], 0, v[210:211]
	s_and_b64 vcc, exec, s[12:13]
	s_waitcnt lgkmcnt(0)
	global_store_dwordx4 v[38:39], v[34:37], off
	s_cbranch_vccnz .LBB0_520
	v_lshlrev_b32_e32 v43, 16, v34
	v_and_b32_e32 v34, 0xffff0000, v34
	v_fma_f32 v43, v43, v43, 0
	v_fmac_f32_e32 v43, v34, v34
	v_lshlrev_b32_e32 v34, 16, v35
	v_and_b32_e32 v35, 0xffff0000, v35
	v_fmac_f32_e32 v43, v34, v34
	v_fmac_f32_e32 v43, v35, v35
	v_lshlrev_b32_e32 v34, 16, v36
	v_and_b32_e32 v35, 0xffff0000, v36
	v_fmac_f32_e32 v43, v34, v34
	v_fmac_f32_e32 v43, v35, v35
	v_lshlrev_b32_e32 v34, 16, v37
	v_and_b32_e32 v35, 0xffff0000, v37
	v_fmac_f32_e32 v43, v34, v34
	v_fmac_f32_e32 v43, v35, v35
	s_nop 1
	v_add_f32_dpp v34, v43, v43 quad_perm:[1,0,3,2] row_mask:0xf bank_mask:0xf
	s_waitcnt lgkmcnt(0)
	s_nop 1
	v_add_f32_dpp v34, v34, v34 quad_perm:[2,3,0,1] row_mask:0xf bank_mask:0xf
	s_nop 1
	v_add_f32_dpp v34, v34, v34 row_half_mirror row_mask:0xf bank_mask:0xf
	v_max_f32_e32 v35, v72, v72
	v_max_f32_e32 v72, v35, v34
.LBB0_520:
	ds_read_b128 v[34:37], v66 offset:1024
	v_add_co_u32_e32 v44, vcc, 0x4000, v38
	s_nop 1
	v_addc_co_u32_e32 v45, vcc, 0, v39, vcc
	s_and_b64 vcc, exec, s[12:13]
	s_waitcnt lgkmcnt(0)
	global_store_dwordx4 v[44:45], v[34:37], off
	s_cbranch_vccnz .LBB0_522
	v_lshlrev_b32_e32 v43, 16, v34
	v_and_b32_e32 v34, 0xffff0000, v34
	v_fma_f32 v43, v43, v43, 0
	v_fmac_f32_e32 v43, v34, v34
	v_lshlrev_b32_e32 v34, 16, v35
	v_and_b32_e32 v35, 0xffff0000, v35
	v_fmac_f32_e32 v43, v34, v34
	v_fmac_f32_e32 v43, v35, v35
	v_lshlrev_b32_e32 v34, 16, v36
	v_and_b32_e32 v35, 0xffff0000, v36
	v_fmac_f32_e32 v43, v34, v34
	v_fmac_f32_e32 v43, v35, v35
	v_lshlrev_b32_e32 v34, 16, v37
	v_and_b32_e32 v35, 0xffff0000, v37
	v_fmac_f32_e32 v43, v34, v34
	v_fmac_f32_e32 v43, v35, v35
	s_nop 1
	v_add_f32_dpp v34, v43, v43 quad_perm:[1,0,3,2] row_mask:0xf bank_mask:0xf
	s_waitcnt lgkmcnt(0)
	s_nop 1
	v_add_f32_dpp v34, v34, v34 quad_perm:[2,3,0,1] row_mask:0xf bank_mask:0xf
	s_nop 1
	v_add_f32_dpp v34, v34, v34 row_half_mirror row_mask:0xf bank_mask:0xf
	v_max_f32_e32 v35, v72, v72
	v_max_f32_e32 v72, v35, v34
.LBB0_522:
	s_nop 0
	v_pk_mul_f32 v[34:35], v[114:115], v[110:111]
	v_pk_mul_f32 v[36:37], v[114:115], v[112:113]
	v_cvt_pk_bf16_f32 v34, v34, v35
	v_cvt_pk_bf16_f32 v35, v36, v37
	s_waitcnt lgkmcnt(0)
	ds_write_b64 v46, v[34:35]
	v_pk_mul_f32 v[34:35], v[114:115], v[106:107]
	v_pk_mul_f32 v[36:37], v[114:115], v[108:109]
	v_cvt_pk_bf16_f32 v34, v34, v35
	v_cvt_pk_bf16_f32 v35, v36, v37
	ds_write_b64 v42, v[34:35]
	v_pk_mul_f32 v[34:35], v[114:115], v[102:103]
	v_pk_mul_f32 v[36:37], v[114:115], v[104:105]
	v_cvt_pk_bf16_f32 v34, v34, v35
	v_cvt_pk_bf16_f32 v35, v36, v37
	ds_write_b64 v40, v[34:35]
	v_pk_mul_f32 v[34:35], v[114:115], v[98:99]
	v_pk_mul_f32 v[36:37], v[114:115], v[100:101]
	v_cvt_pk_bf16_f32 v34, v34, v35
	v_cvt_pk_bf16_f32 v35, v36, v37
	ds_write_b64 v41, v[34:35]
	s_waitcnt lgkmcnt(0)
	ds_read_b128 v[34:37], v66
	s_and_b64 vcc, exec, s[12:13]
	s_waitcnt lgkmcnt(0)
	global_store_dwordx4 v[38:39], v[34:37], off offset:128
	s_cbranch_vccnz .LBB0_524
	v_lshlrev_b32_e32 v40, 16, v34
	v_and_b32_e32 v34, 0xffff0000, v34
	v_fma_f32 v40, v40, v40, 0
	v_fmac_f32_e32 v40, v34, v34
	v_lshlrev_b32_e32 v34, 16, v35
	v_and_b32_e32 v35, 0xffff0000, v35
	v_fmac_f32_e32 v40, v34, v34
	v_fmac_f32_e32 v40, v35, v35
	v_lshlrev_b32_e32 v34, 16, v36
	v_and_b32_e32 v35, 0xffff0000, v36
	v_fmac_f32_e32 v40, v34, v34
	v_fmac_f32_e32 v40, v35, v35
	v_lshlrev_b32_e32 v34, 16, v37
	v_and_b32_e32 v35, 0xffff0000, v37
	v_fmac_f32_e32 v40, v34, v34
	v_fmac_f32_e32 v40, v35, v35
	s_nop 1
	v_add_f32_dpp v34, v40, v40 quad_perm:[1,0,3,2] row_mask:0xf bank_mask:0xf
	s_waitcnt lgkmcnt(0)
	s_nop 1
	v_add_f32_dpp v34, v34, v34 quad_perm:[2,3,0,1] row_mask:0xf bank_mask:0xf
	s_nop 1
	v_add_f32_dpp v34, v34, v34 row_half_mirror row_mask:0xf bank_mask:0xf
	v_max_f32_e32 v35, v73, v73
	v_max_f32_e32 v73, v35, v34
.LBB0_524:
	ds_read_b128 v[34:37], v66 offset:1024
	v_add_co_u32_e32 v38, vcc, 0x4000, v38
	s_nop 1
	v_addc_co_u32_e32 v39, vcc, 0, v39, vcc
	s_and_b64 vcc, exec, s[12:13]
	s_waitcnt lgkmcnt(0)
	global_store_dwordx4 v[38:39], v[34:37], off offset:128
	s_cbranch_vccnz .LBB0_526
	v_lshlrev_b32_e32 v38, 16, v34
	v_and_b32_e32 v34, 0xffff0000, v34
	v_fma_f32 v38, v38, v38, 0
	v_fmac_f32_e32 v38, v34, v34
	v_lshlrev_b32_e32 v34, 16, v35
	v_and_b32_e32 v35, 0xffff0000, v35
	v_fmac_f32_e32 v38, v34, v34
	v_fmac_f32_e32 v38, v35, v35
	v_lshlrev_b32_e32 v34, 16, v36
	v_and_b32_e32 v35, 0xffff0000, v36
	v_fmac_f32_e32 v38, v34, v34
	v_fmac_f32_e32 v38, v35, v35
	v_lshlrev_b32_e32 v34, 16, v37
	v_and_b32_e32 v35, 0xffff0000, v37
	v_fmac_f32_e32 v38, v34, v34
	v_fmac_f32_e32 v38, v35, v35
	s_nop 1
	v_add_f32_dpp v34, v38, v38 quad_perm:[1,0,3,2] row_mask:0xf bank_mask:0xf
	s_waitcnt lgkmcnt(0)
	s_nop 1
	v_add_f32_dpp v34, v34, v34 quad_perm:[2,3,0,1] row_mask:0xf bank_mask:0xf
	s_nop 1
	v_add_f32_dpp v34, v34, v34 row_half_mirror row_mask:0xf bank_mask:0xf
	v_max_f32_e32 v35, v73, v73
	v_max_f32_e32 v73, v35, v34
.LBB0_526:
	v_mov_b32_e32 v40, v229
	s_waitcnt lgkmcnt(0)
	v_pk_mul_f32 v[30:31], v[114:115], v[30:31]
	v_bfe_u32 v38, v40, 3, 3
	v_or_b32_e32 v34, s65, v38
	v_ashrrev_i32_e32 v35, 31, v34
	v_lshlrev_b64 v[36:37], 11, v[34:35]
	v_lshlrev_b32_e32 v34, 7, v40
	v_lshrrev_b32_e32 v39, 1, v40
	v_and_b32_e32 v34, 0x780, v34
	v_and_b32_e32 v39, 8, v39
	v_add3_u32 v42, s73, v34, v39
	v_lshl_add_u32 v34, v38, 7, s73
	v_bitop3_b32 v38, v38, v40, 7 bitop3:0x78
	v_lshlrev_b32_e32 v38, 4, v38
	v_pk_mul_f32 v[26:27], v[114:115], v[26:27]
	v_and_b32_e32 v35, 7, v40
	v_bfe_u32 v41, v40, 5, 1
	v_add_u32_e32 v34, v34, v38
	v_cvt_pk_bf16_f32 v38, v30, v31
	v_pk_mul_f32 v[30:31], v[114:115], v[32:33]
	v_cvt_pk_bf16_f32 v32, v26, v27
	v_pk_mul_f32 v[26:27], v[114:115], v[28:29]
	v_pk_mul_f32 v[22:23], v[114:115], v[22:23]
	v_pk_mul_f32 v[24:25], v[114:115], v[24:25]
	v_pk_mul_f32 v[18:19], v[114:115], v[18:19]
	v_pk_mul_f32 v[20:21], v[114:115], v[20:21]
	v_cvt_pk_bf16_f32 v39, v30, v31
	v_bitop3_b32 v30, v41, v40, 7 bitop3:0x78
	v_cvt_pk_bf16_f32 v33, v26, v27
	v_bitop3_b32 v26, v41, v35, 2 bitop3:0x36
	v_cvt_pk_bf16_f32 v22, v22, v23
	v_cvt_pk_bf16_f32 v23, v24, v25
	v_bitop3_b32 v24, v41, v35, 4 bitop3:0x36
	v_cvt_pk_bf16_f32 v18, v18, v19
	v_cvt_pk_bf16_f32 v19, v20, v21
	v_bitop3_b32 v20, v41, v35, 6 bitop3:0x36
	v_lshlrev_b32_e32 v30, 4, v30
	v_lshlrev_b32_e32 v26, 4, v26
	v_lshlrev_b32_e32 v24, 4, v24
	v_lshlrev_b32_e32 v20, 4, v20
	v_add_u32_e32 v30, v42, v30
	v_add_u32_e32 v26, v42, v26
	v_add_u32_e32 v24, v42, v24
	v_add_u32_e32 v25, v42, v20
	ds_write_b64 v30, v[38:39]
	ds_write_b64 v26, v[32:33]
	ds_write_b64 v24, v[22:23]
	ds_write_b64 v25, v[18:19]
	s_waitcnt lgkmcnt(0)
	ds_read_b128 v[18:21], v34
	v_lshl_add_u64 v[22:23], s[88:89], 0, v[36:37]
	v_lshlrev_b32_e32 v210, 4, v35
	v_lshl_add_u64 v[22:23], v[22:23], 0, v[210:211]
	s_and_b64 vcc, exec, s[12:13]
	s_waitcnt lgkmcnt(0)
	global_store_dwordx4 v[22:23], v[18:21], off
	s_cbranch_vccnz .LBB0_528
	v_lshlrev_b32_e32 v27, 16, v18
	v_and_b32_e32 v18, 0xffff0000, v18
	v_fma_f32 v27, v27, v27, 0
	v_fmac_f32_e32 v27, v18, v18
	v_lshlrev_b32_e32 v18, 16, v19
	v_and_b32_e32 v19, 0xffff0000, v19
	v_fmac_f32_e32 v27, v18, v18
	v_fmac_f32_e32 v27, v19, v19
	v_lshlrev_b32_e32 v18, 16, v20
	v_and_b32_e32 v19, 0xffff0000, v20
	v_fmac_f32_e32 v27, v18, v18
	v_fmac_f32_e32 v27, v19, v19
	v_lshlrev_b32_e32 v18, 16, v21
	v_and_b32_e32 v19, 0xffff0000, v21
	v_fmac_f32_e32 v27, v18, v18
	v_fmac_f32_e32 v27, v19, v19
	s_nop 1
	v_add_f32_dpp v18, v27, v27 quad_perm:[1,0,3,2] row_mask:0xf bank_mask:0xf
	s_waitcnt lgkmcnt(0)
	s_nop 1
	v_add_f32_dpp v18, v18, v18 quad_perm:[2,3,0,1] row_mask:0xf bank_mask:0xf
	s_nop 1
	v_add_f32_dpp v18, v18, v18 row_half_mirror row_mask:0xf bank_mask:0xf
	v_max_f32_e32 v19, v72, v72
	v_max_f32_e32 v72, v19, v18
.LBB0_528:
	ds_read_b128 v[18:21], v34 offset:1024
	v_add_co_u32_e32 v28, vcc, 0x4000, v22
	s_nop 1
	v_addc_co_u32_e32 v29, vcc, 0, v23, vcc
	s_and_b64 vcc, exec, s[12:13]
	s_waitcnt lgkmcnt(0)
	global_store_dwordx4 v[28:29], v[18:21], off
	s_cbranch_vccnz .LBB0_530
	v_lshlrev_b32_e32 v27, 16, v18
	v_and_b32_e32 v18, 0xffff0000, v18
	v_fma_f32 v27, v27, v27, 0
	v_fmac_f32_e32 v27, v18, v18
	v_lshlrev_b32_e32 v18, 16, v19
	v_and_b32_e32 v19, 0xffff0000, v19
	v_fmac_f32_e32 v27, v18, v18
	v_fmac_f32_e32 v27, v19, v19
	v_lshlrev_b32_e32 v18, 16, v20
	v_and_b32_e32 v19, 0xffff0000, v20
	v_fmac_f32_e32 v27, v18, v18
	v_fmac_f32_e32 v27, v19, v19
	v_lshlrev_b32_e32 v18, 16, v21
	v_and_b32_e32 v19, 0xffff0000, v21
	v_fmac_f32_e32 v27, v18, v18
	v_fmac_f32_e32 v27, v19, v19
	s_nop 1
	v_add_f32_dpp v18, v27, v27 quad_perm:[1,0,3,2] row_mask:0xf bank_mask:0xf
	s_waitcnt lgkmcnt(0)
	s_nop 1
	v_add_f32_dpp v18, v18, v18 quad_perm:[2,3,0,1] row_mask:0xf bank_mask:0xf
	s_nop 1
	v_add_f32_dpp v18, v18, v18 row_half_mirror row_mask:0xf bank_mask:0xf
	v_max_f32_e32 v19, v72, v72
	v_max_f32_e32 v72, v19, v18
.LBB0_530:
	s_nop 0
	v_pk_mul_f32 v[18:19], v[114:115], v[94:95]
	v_pk_mul_f32 v[20:21], v[114:115], v[96:97]
	v_cvt_pk_bf16_f32 v18, v18, v19
	v_cvt_pk_bf16_f32 v19, v20, v21
	s_waitcnt lgkmcnt(0)
	ds_write_b64 v30, v[18:19]
	v_pk_mul_f32 v[18:19], v[114:115], v[90:91]
	v_pk_mul_f32 v[20:21], v[114:115], v[92:93]
	v_cvt_pk_bf16_f32 v18, v18, v19
	v_cvt_pk_bf16_f32 v19, v20, v21
	ds_write_b64 v26, v[18:19]
	v_pk_mul_f32 v[18:19], v[114:115], v[86:87]
	v_pk_mul_f32 v[20:21], v[114:115], v[88:89]
	v_cvt_pk_bf16_f32 v18, v18, v19
	v_cvt_pk_bf16_f32 v19, v20, v21
	ds_write_b64 v24, v[18:19]
	v_pk_mul_f32 v[18:19], v[114:115], v[82:83]
	v_pk_mul_f32 v[20:21], v[114:115], v[84:85]
	v_cvt_pk_bf16_f32 v18, v18, v19
	v_cvt_pk_bf16_f32 v19, v20, v21
	ds_write_b64 v25, v[18:19]
	s_waitcnt lgkmcnt(0)
	ds_read_b128 v[18:21], v34
	s_and_b64 vcc, exec, s[12:13]
	s_waitcnt lgkmcnt(0)
	global_store_dwordx4 v[22:23], v[18:21], off offset:128
	s_cbranch_vccnz .LBB0_532
	v_lshlrev_b32_e32 v24, 16, v18
	v_and_b32_e32 v18, 0xffff0000, v18
	v_fma_f32 v24, v24, v24, 0
	v_fmac_f32_e32 v24, v18, v18
	v_lshlrev_b32_e32 v18, 16, v19
	v_and_b32_e32 v19, 0xffff0000, v19
	v_fmac_f32_e32 v24, v18, v18
	v_fmac_f32_e32 v24, v19, v19
	v_lshlrev_b32_e32 v18, 16, v20
	v_and_b32_e32 v19, 0xffff0000, v20
	v_fmac_f32_e32 v24, v18, v18
	v_fmac_f32_e32 v24, v19, v19
	v_lshlrev_b32_e32 v18, 16, v21
	v_and_b32_e32 v19, 0xffff0000, v21
	v_fmac_f32_e32 v24, v18, v18
	v_fmac_f32_e32 v24, v19, v19
	s_nop 1
	v_add_f32_dpp v18, v24, v24 quad_perm:[1,0,3,2] row_mask:0xf bank_mask:0xf
	s_waitcnt lgkmcnt(0)
	s_nop 1
	v_add_f32_dpp v18, v18, v18 quad_perm:[2,3,0,1] row_mask:0xf bank_mask:0xf
	s_nop 1
	v_add_f32_dpp v18, v18, v18 row_half_mirror row_mask:0xf bank_mask:0xf
	v_max_f32_e32 v19, v73, v73
	v_max_f32_e32 v73, v19, v18
.LBB0_532:
	ds_read_b128 v[18:21], v34 offset:1024
	v_add_co_u32_e32 v22, vcc, 0x4000, v22
	s_nop 1
	v_addc_co_u32_e32 v23, vcc, 0, v23, vcc
	s_and_b64 vcc, exec, s[12:13]
	s_waitcnt lgkmcnt(0)
	global_store_dwordx4 v[22:23], v[18:21], off offset:128
	s_cbranch_vccnz .LBB0_534
	v_lshlrev_b32_e32 v22, 16, v18
	v_and_b32_e32 v18, 0xffff0000, v18
	v_fma_f32 v22, v22, v22, 0
	v_fmac_f32_e32 v22, v18, v18
	v_lshlrev_b32_e32 v18, 16, v19
	v_and_b32_e32 v19, 0xffff0000, v19
	v_fmac_f32_e32 v22, v18, v18
	v_fmac_f32_e32 v22, v19, v19
	v_lshlrev_b32_e32 v18, 16, v20
	v_and_b32_e32 v19, 0xffff0000, v20
	v_fmac_f32_e32 v22, v18, v18
	v_fmac_f32_e32 v22, v19, v19
	v_lshlrev_b32_e32 v18, 16, v21
	v_and_b32_e32 v19, 0xffff0000, v21
	v_fmac_f32_e32 v22, v18, v18
	v_fmac_f32_e32 v22, v19, v19
	s_nop 1
	v_add_f32_dpp v18, v22, v22 quad_perm:[1,0,3,2] row_mask:0xf bank_mask:0xf
	s_waitcnt lgkmcnt(0)
	s_nop 1
	v_add_f32_dpp v18, v18, v18 quad_perm:[2,3,0,1] row_mask:0xf bank_mask:0xf
	s_nop 1
	v_add_f32_dpp v18, v18, v18 row_half_mirror row_mask:0xf bank_mask:0xf
	v_max_f32_e32 v19, v73, v73
	v_max_f32_e32 v73, v19, v18
.LBB0_534:
	v_mov_b32_e32 v24, v229
	s_waitcnt lgkmcnt(0)
	v_pk_mul_f32 v[14:15], v[114:115], v[14:15]
	v_bfe_u32 v22, v24, 3, 3
	v_or_b32_e32 v18, s70, v22
	v_ashrrev_i32_e32 v19, 31, v18
	v_lshlrev_b64 v[20:21], 11, v[18:19]
	v_lshlrev_b32_e32 v18, 7, v24
	v_lshrrev_b32_e32 v23, 1, v24
	v_and_b32_e32 v18, 0x780, v18
	v_and_b32_e32 v23, 8, v23
	v_add3_u32 v26, s73, v18, v23
	v_lshl_add_u32 v18, v22, 7, s73
	v_bitop3_b32 v22, v22, v24, 7 bitop3:0x78
	v_lshlrev_b32_e32 v22, 4, v22
	v_pk_mul_f32 v[10:11], v[114:115], v[10:11]
	v_and_b32_e32 v19, 7, v24
	v_bfe_u32 v25, v24, 5, 1
	v_add_u32_e32 v18, v18, v22
	v_cvt_pk_bf16_f32 v22, v14, v15
	v_pk_mul_f32 v[14:15], v[114:115], v[16:17]
	v_cvt_pk_bf16_f32 v16, v10, v11
	v_pk_mul_f32 v[10:11], v[114:115], v[12:13]
	v_pk_mul_f32 v[6:7], v[114:115], v[6:7]
	v_pk_mul_f32 v[8:9], v[114:115], v[8:9]
	v_pk_mul_f32 v[2:3], v[114:115], v[2:3]
	v_pk_mul_f32 v[4:5], v[114:115], v[4:5]
	v_cvt_pk_bf16_f32 v23, v14, v15
	v_bitop3_b32 v14, v25, v24, 7 bitop3:0x78
	v_cvt_pk_bf16_f32 v17, v10, v11
	v_bitop3_b32 v10, v25, v19, 2 bitop3:0x36
	v_cvt_pk_bf16_f32 v6, v6, v7
	v_cvt_pk_bf16_f32 v7, v8, v9
	v_bitop3_b32 v8, v25, v19, 4 bitop3:0x36
	v_cvt_pk_bf16_f32 v2, v2, v3
	v_cvt_pk_bf16_f32 v3, v4, v5
	v_bitop3_b32 v4, v25, v19, 6 bitop3:0x36
	v_lshlrev_b32_e32 v14, 4, v14
	v_lshlrev_b32_e32 v10, 4, v10
	v_lshlrev_b32_e32 v8, 4, v8
	v_lshlrev_b32_e32 v4, 4, v4
	v_add_u32_e32 v14, v26, v14
	v_add_u32_e32 v10, v26, v10
	v_add_u32_e32 v8, v26, v8
	v_add_u32_e32 v9, v26, v4
	ds_write_b64 v14, v[22:23]
	ds_write_b64 v10, v[16:17]
	ds_write_b64 v8, v[6:7]
	ds_write_b64 v9, v[2:3]
	s_waitcnt lgkmcnt(0)
	ds_read_b128 v[2:5], v18
	v_lshl_add_u64 v[6:7], s[88:89], 0, v[20:21]
	v_lshlrev_b32_e32 v210, 4, v19
	v_lshl_add_u64 v[6:7], v[6:7], 0, v[210:211]
	s_and_b64 vcc, exec, s[12:13]
	s_waitcnt lgkmcnt(0)
	global_store_dwordx4 v[6:7], v[2:5], off
	s_cbranch_vccnz .LBB0_536
	v_lshlrev_b32_e32 v11, 16, v2
	v_and_b32_e32 v2, 0xffff0000, v2
	v_fma_f32 v11, v11, v11, 0
	v_fmac_f32_e32 v11, v2, v2
	v_lshlrev_b32_e32 v2, 16, v3
	v_and_b32_e32 v3, 0xffff0000, v3
	v_fmac_f32_e32 v11, v2, v2
	v_fmac_f32_e32 v11, v3, v3
	v_lshlrev_b32_e32 v2, 16, v4
	v_and_b32_e32 v3, 0xffff0000, v4
	v_fmac_f32_e32 v11, v2, v2
	v_fmac_f32_e32 v11, v3, v3
	v_lshlrev_b32_e32 v2, 16, v5
	v_and_b32_e32 v3, 0xffff0000, v5
	v_fmac_f32_e32 v11, v2, v2
	v_fmac_f32_e32 v11, v3, v3
	s_nop 1
	v_add_f32_dpp v2, v11, v11 quad_perm:[1,0,3,2] row_mask:0xf bank_mask:0xf
	s_waitcnt lgkmcnt(0)
	s_nop 1
	v_add_f32_dpp v2, v2, v2 quad_perm:[2,3,0,1] row_mask:0xf bank_mask:0xf
	s_nop 1
	v_add_f32_dpp v2, v2, v2 row_half_mirror row_mask:0xf bank_mask:0xf
	v_max_f32_e32 v3, v72, v72
	v_max_f32_e32 v72, v3, v2
.LBB0_536:
	ds_read_b128 v[2:5], v18 offset:1024
	v_add_co_u32_e32 v12, vcc, 0x4000, v6
	s_nop 1
	v_addc_co_u32_e32 v13, vcc, 0, v7, vcc
	s_and_b64 vcc, exec, s[12:13]
	s_waitcnt lgkmcnt(0)
	global_store_dwordx4 v[12:13], v[2:5], off
	s_cbranch_vccnz .LBB0_538
	v_lshlrev_b32_e32 v11, 16, v2
	v_and_b32_e32 v2, 0xffff0000, v2
	v_fma_f32 v11, v11, v11, 0
	v_fmac_f32_e32 v11, v2, v2
	v_lshlrev_b32_e32 v2, 16, v3
	v_and_b32_e32 v3, 0xffff0000, v3
	v_fmac_f32_e32 v11, v2, v2
	v_fmac_f32_e32 v11, v3, v3
	v_lshlrev_b32_e32 v2, 16, v4
	v_and_b32_e32 v3, 0xffff0000, v4
	v_fmac_f32_e32 v11, v2, v2
	v_fmac_f32_e32 v11, v3, v3
	v_lshlrev_b32_e32 v2, 16, v5
	v_and_b32_e32 v3, 0xffff0000, v5
	v_fmac_f32_e32 v11, v2, v2
	v_fmac_f32_e32 v11, v3, v3
	s_nop 1
	v_add_f32_dpp v2, v11, v11 quad_perm:[1,0,3,2] row_mask:0xf bank_mask:0xf
	s_waitcnt lgkmcnt(0)
	s_nop 1
	v_add_f32_dpp v2, v2, v2 quad_perm:[2,3,0,1] row_mask:0xf bank_mask:0xf
	s_nop 1
	v_add_f32_dpp v2, v2, v2 row_half_mirror row_mask:0xf bank_mask:0xf
	v_max_f32_e32 v3, v72, v72
	v_max_f32_e32 v72, v3, v2
.LBB0_538:
	s_nop 0
	v_pk_mul_f32 v[2:3], v[114:115], v[62:63]
	v_pk_mul_f32 v[4:5], v[114:115], v[64:65]
	v_cvt_pk_bf16_f32 v2, v2, v3
	v_cvt_pk_bf16_f32 v3, v4, v5
	s_waitcnt lgkmcnt(0)
	ds_write_b64 v14, v[2:3]
	v_pk_mul_f32 v[2:3], v[114:115], v[58:59]
	v_pk_mul_f32 v[4:5], v[114:115], v[60:61]
	v_cvt_pk_bf16_f32 v2, v2, v3
	v_cvt_pk_bf16_f32 v3, v4, v5
	ds_write_b64 v10, v[2:3]
	v_pk_mul_f32 v[2:3], v[114:115], v[54:55]
	v_pk_mul_f32 v[4:5], v[114:115], v[56:57]
	v_cvt_pk_bf16_f32 v2, v2, v3
	v_cvt_pk_bf16_f32 v3, v4, v5
	ds_write_b64 v8, v[2:3]
	v_pk_mul_f32 v[2:3], v[114:115], v[50:51]
	v_pk_mul_f32 v[4:5], v[114:115], v[52:53]
	v_cvt_pk_bf16_f32 v2, v2, v3
	v_cvt_pk_bf16_f32 v3, v4, v5
	ds_write_b64 v9, v[2:3]
	s_waitcnt lgkmcnt(0)
	ds_read_b128 v[2:5], v18
	s_and_b64 vcc, exec, s[12:13]
	s_waitcnt lgkmcnt(0)
	global_store_dwordx4 v[6:7], v[2:5], off offset:128
	s_cbranch_vccnz .LBB0_540
	v_lshlrev_b32_e32 v8, 16, v2
	v_and_b32_e32 v2, 0xffff0000, v2
	v_fma_f32 v8, v8, v8, 0
	v_fmac_f32_e32 v8, v2, v2
	v_lshlrev_b32_e32 v2, 16, v3
	v_and_b32_e32 v3, 0xffff0000, v3
	v_fmac_f32_e32 v8, v2, v2
	v_fmac_f32_e32 v8, v3, v3
	v_lshlrev_b32_e32 v2, 16, v4
	v_and_b32_e32 v3, 0xffff0000, v4
	v_fmac_f32_e32 v8, v2, v2
	v_fmac_f32_e32 v8, v3, v3
	v_lshlrev_b32_e32 v2, 16, v5
	v_and_b32_e32 v3, 0xffff0000, v5
	v_fmac_f32_e32 v8, v2, v2
	v_fmac_f32_e32 v8, v3, v3
	s_nop 1
	v_add_f32_dpp v2, v8, v8 quad_perm:[1,0,3,2] row_mask:0xf bank_mask:0xf
	s_waitcnt lgkmcnt(0)
	s_nop 1
	v_add_f32_dpp v2, v2, v2 quad_perm:[2,3,0,1] row_mask:0xf bank_mask:0xf
	s_nop 1
	v_add_f32_dpp v2, v2, v2 row_half_mirror row_mask:0xf bank_mask:0xf
	v_max_f32_e32 v3, v73, v73
	v_max_f32_e32 v73, v3, v2
.LBB0_540:
	ds_read_b128 v[2:5], v18 offset:1024
	v_add_co_u32_e32 v6, vcc, 0x4000, v6
	s_nop 1
	v_addc_co_u32_e32 v7, vcc, 0, v7, vcc
	s_and_b64 vcc, exec, s[12:13]
	s_waitcnt lgkmcnt(0)
	global_store_dwordx4 v[6:7], v[2:5], off offset:128
	s_cbranch_vccnz .LBB0_542
	v_lshlrev_b32_e32 v6, 16, v2
	v_and_b32_e32 v2, 0xffff0000, v2
	v_fma_f32 v6, v6, v6, 0
	v_fmac_f32_e32 v6, v2, v2
	v_lshlrev_b32_e32 v2, 16, v3
	v_and_b32_e32 v3, 0xffff0000, v3
	v_fmac_f32_e32 v6, v2, v2
	v_fmac_f32_e32 v6, v3, v3
	v_lshlrev_b32_e32 v2, 16, v4
	v_and_b32_e32 v3, 0xffff0000, v4
	v_fmac_f32_e32 v6, v2, v2
	v_fmac_f32_e32 v6, v3, v3
	v_lshlrev_b32_e32 v2, 16, v5
	v_and_b32_e32 v3, 0xffff0000, v5
	v_fmac_f32_e32 v6, v2, v2
	v_fmac_f32_e32 v6, v3, v3
	s_nop 1
	v_add_f32_dpp v2, v6, v6 quad_perm:[1,0,3,2] row_mask:0xf bank_mask:0xf
	s_waitcnt lgkmcnt(0)
	s_nop 1
	v_add_f32_dpp v2, v2, v2 quad_perm:[2,3,0,1] row_mask:0xf bank_mask:0xf
	s_nop 1
	v_add_f32_dpp v2, v2, v2 row_half_mirror row_mask:0xf bank_mask:0xf
	v_max_f32_e32 v3, v73, v73
	v_max_f32_e32 v73, v3, v2

.LBB0_864:
	v_readlane_b32 s7, v254, 0
	s_lshr_b32 s5, s7, 2
	s_and_b32 s4, s7, 7
	s_and_b32 s5, s5, 0x3ffffff8
	s_or_b32 s4, s5, s4
	s_sub_i32 s5, 63, s4
	s_lshl_b32 s4, s4, 2
	s_add_i32 s4, s4, 0
	s_add_i32 s6, s4, 0x21400
	v_mov_b32_e32 v2, s6
	s_waitcnt lgkmcnt(0)
	s_barrier
	ds_read_b32 v2, v2
	s_lshl_b32 s5, s5, 2
	s_add_i32 s5, s5, 0
	s_add_i32 s4, s4, 0x21600
	s_add_i32 s6, s5, 0x21500
	v_mov_b32_e32 v4, s4
	s_add_i32 s4, s5, 0x21700
	v_mov_b32_e32 v3, s6
	v_mov_b32_e32 v5, s4
	ds_read_b32 v3, v3
	ds_read_b32 v4, v4
	ds_read_b32 v5, v5
	s_waitcnt lgkmcnt(3)
	v_readfirstlane_b32 s33, v2
	s_lshl_b32 s4, s33, 2
	s_add_i32 s5, 0, 0x21000
	s_add_i32 s4, s5, s4
	s_waitcnt lgkmcnt(2)
	v_readfirstlane_b32 s52, v3
	v_mov_b32_e32 v2, s4
	s_lshl_b32 s4, s52, 2
	s_add_i32 s4, s5, s4
	s_waitcnt lgkmcnt(1)
	v_readfirstlane_b32 s53, v4
	v_mov_b32_e32 v3, s4
	s_lshl_b32 s4, s53, 2
	s_add_i32 s4, s5, s4
	s_waitcnt lgkmcnt(0)
	v_readfirstlane_b32 s54, v5
	v_mov_b32_e32 v4, s4
	s_lshl_b32 s4, s54, 2
	s_add_i32 s4, s5, s4
	v_mov_b32_e32 v5, s4
	ds_read_b32 v2, v2
	ds_read_b32 v3, v3
	ds_read_b32 v4, v4
	ds_read_b32 v5, v5
	s_waitcnt lgkmcnt(0)
	s_barrier
	s_load_dwordx4 s[16:19], s[0:1], 0x120
	s_load_dwordx2 s[10:11], s[0:1], 0x140
	s_bfe_u32 s12, s7, 0x20003
	s_bitcmp0_b32 s7, 5
	s_load_dwordx2 s[6:7], s[0:1], 0x58
	s_load_dwordx2 s[8:9], s[0:1], 0xe8
	s_cselect_b64 s[4:5], -1, 0
	s_lshl_b32 s13, s12, 8
	s_add_i32 s14, s13, 0x300
	s_lshl_b32 s12, s12, 7
	s_waitcnt lgkmcnt(0)
	s_add_u32 s20, s10, s12
	s_mov_b32 s55, 0
	v_readfirstlane_b32 s56, v2
	v_readfirstlane_b32 s57, v3
	v_readfirstlane_b32 s58, v4
	v_readfirstlane_b32 s59, v5
	s_addc_u32 s21, s11, 0
	v_mov_b32_e32 v163, 0
	v_lshlrev_b32_e64 v244, 2, s33
	v_lshlrev_b32_e64 v245, 2, s52
	v_lshlrev_b32_e64 v246, 2, s53
	v_lshlrev_b32_e64 v247, 2, s54
	global_load_dword v244, v244, s[2:3] offset:1024
	global_load_dword v245, v245, s[2:3] offset:1024
	global_load_dword v246, v246, s[2:3] offset:1024
	global_load_dword v247, v247, s[2:3] offset:1024
	s_waitcnt vmcnt(0)
	v_readfirstlane_b32 s98, v244
	v_readfirstlane_b32 s99, v245
	v_readfirstlane_b32 s100, v246
	v_readfirstlane_b32 s101, v247
	s_movk_i32 s60, 0xf800
	v_mov_b32_e32 v166, s14
	v_mov_b32_e32 v167, s13
	s_add_i32 s61, 0, 0x20000
	s_branch .LBB0_866

.LBB0_866:
	s_sub_i32 s12, 3, s55
	s_and_b64 s[10:11], s[4:5], exec
	s_cselect_b32 s22, s55, s12
	s_cmp_eq_u32 s22, 2
	s_cselect_b64 s[12:13], -1, 0
	s_and_b64 s[10:11], s[12:13], exec
	s_cselect_b32 s23, s53, s54
	s_cmp_eq_u32 s22, 1
	s_cselect_b64 s[14:15], -1, 0
	s_and_b64 s[10:11], s[14:15], exec
	s_cselect_b32 s24, s52, s23
	s_cmp_eq_u32 s22, 0
	s_cselect_b64 s[22:23], -1, 0
	s_and_b64 s[10:11], s[22:23], exec
	s_cselect_b32 s10, s33, s24
	s_ashr_i32 s11, s10, 31
	s_and_b64 s[24:25], s[12:13], exec
	s_cselect_b32 s62, s100, s101
	s_and_b64 s[24:25], s[14:15], exec
	s_cselect_b32 s62, s99, s62
	s_and_b64 s[24:25], s[22:23], exec
	s_cselect_b32 s62, s98, s62
	s_cmp_lt_i32 s62, 1
	s_cbranch_scc1 .LBB0_865
	s_and_b64 s[12:13], s[12:13], exec
	s_cselect_b32 s24, s58, s59
	s_and_b64 s[12:13], s[14:15], exec
	s_cselect_b32 s14, s57, s24
	s_and_b64 s[12:13], s[22:23], exec
	s_cselect_b32 s63, s56, s14
	s_lshl_b64 s[12:13], s[10:11], 21
	s_add_u32 s12, s6, s12
	s_addc_u32 s13, s7, s13
	s_add_u32 s22, s12, 0x20000000
	s_addc_u32 s23, s13, 0
	s_lshl_b64 s[10:11], s[10:11], 16
	s_add_u32 s24, s16, s10
	s_addc_u32 s25, s17, s11
	s_add_u32 s26, s18, s10
	s_addc_u32 s27, s19, s11
	s_add_u32 s28, s12, 0x20001000
	s_addc_u32 s29, s13, 0
	s_add_u32 s30, s12, 0x20020000
	s_addc_u32 s31, s13, 0
	s_add_u32 s34, s12, 0x20021000
	s_addc_u32 s35, s13, 0
	s_add_u32 s36, s12, 0x20040000
	s_addc_u32 s37, s13, 0
	s_add_u32 s38, s12, 0x20041000
	s_addc_u32 s39, s13, 0
	s_mov_b32 s64, 0
	s_branch .LBB0_869

	.amdhsa_kernel _ZN2nk6k_megaENS_6ParamsE
		.amdhsa_group_segment_fixed_size 0
		.amdhsa_private_segment_fixed_size 0
		.amdhsa_kernarg_size 592
		.amdhsa_user_sgpr_count 2
		.amdhsa_user_sgpr_dispatch_ptr 0
		.amdhsa_user_sgpr_queue_ptr 0
		.amdhsa_user_sgpr_kernarg_segment_ptr 1
		.amdhsa_user_sgpr_dispatch_id 0
		.amdhsa_user_sgpr_kernarg_preload_length 0
		.amdhsa_user_sgpr_kernarg_preload_offset 0
		.amdhsa_user_sgpr_private_segment_size 0
		.amdhsa_uses_dynamic_stack 0
		.amdhsa_enable_private_segment 0
		.amdhsa_system_sgpr_workgroup_id_x 1
		.amdhsa_system_sgpr_workgroup_id_y 0
		.amdhsa_system_sgpr_workgroup_id_z 0
		.amdhsa_system_sgpr_workgroup_info 0
		.amdhsa_system_vgpr_workitem_id 0
		.amdhsa_next_free_vgpr 256
		.amdhsa_next_free_sgpr 102
		.amdhsa_accum_offset 256
		.amdhsa_reserve_vcc 1
		.amdhsa_float_round_mode_32 0
		.amdhsa_float_round_mode_16_64 0
		.amdhsa_float_denorm_mode_32 3
		.amdhsa_float_denorm_mode_16_64 3
		.amdhsa_dx10_clamp 1
		.amdhsa_ieee_mode 1
		.amdhsa_fp16_overflow 0
		.amdhsa_tg_split 0
		.amdhsa_exception_fp_ieee_invalid_op 0
		.amdhsa_exception_fp_denorm_src 0
		.amdhsa_exception_fp_ieee_div_zero 0
		.amdhsa_exception_fp_ieee_overflow 0
		.amdhsa_exception_fp_ieee_underflow 0
		.amdhsa_exception_fp_ieee_inexact 0
		.amdhsa_exception_int_div_zero 0
	.end_amdhsa_kernel

amdhsa.kernels:
  - .agpr_count:     0
    .args:
      - .offset:         0
        .size:           336
        .value_kind:     by_value
      - .offset:         336
        .size:           4
        .value_kind:     hidden_block_count_x
      - .offset:         340
        .size:           4
        .value_kind:     hidden_block_count_y
      - .offset:         344
        .size:           4
        .value_kind:     hidden_block_count_z
      - .offset:         348
        .size:           2
        .value_kind:     hidden_group_size_x
      - .offset:         350
        .size:           2
        .value_kind:     hidden_group_size_y
      - .offset:         352
        .size:           2
        .value_kind:     hidden_group_size_z
      - .offset:         354
        .size:           2
        .value_kind:     hidden_remainder_x
      - .offset:         356
        .size:           2
        .value_kind:     hidden_remainder_y
      - .offset:         358
        .size:           2
        .value_kind:     hidden_remainder_z
      - .offset:         376
        .size:           8
        .value_kind:     hidden_global_offset_x
      - .offset:         384
        .size:           8
        .value_kind:     hidden_global_offset_y
      - .offset:         392
        .size:           8
        .value_kind:     hidden_global_offset_z
      - .offset:         400
        .size:           2
        .value_kind:     hidden_grid_dims
      - .offset:         456
        .size:           4
        .value_kind:     hidden_dynamic_lds_size
    .group_segment_fixed_size: 0
    .kernarg_segment_align: 8
    .kernarg_segment_size: 592
    .language:       OpenCL C
    .language_version:
      - 2
      - 0
    .max_flat_workgroup_size: 512
    .name:           _ZN2nk6k_megaENS_6ParamsE
    .private_segment_fixed_size: 0
    .sgpr_count:     108
    .sgpr_spill_count: 162
    .symbol:         _ZN2nk6k_megaENS_6ParamsE.kd
    .uniform_work_group_size: 1
    .uses_dynamic_stack: false
    .vgpr_count:     256
    .vgpr_spill_count: 0
    .wavefront_size: 64
